# in-projection and expert-down GEMM set-up: the full vmcnt wait before each tile's K-loop became a counted wait that retires only the staged tiles, leaving the previous tile's output stores to drain un
# speedup vs baseline: 1.0055x; 1.0032x over previous
.LBB0_225:
	s_ashr_i32 s43, s42, 31
	s_lshl_b64 s[44:45], s[42:43], 19
	s_add_u32 s44, s12, s44
	s_addc_u32 s45, s13, s45
	s_and_b64 s[46:47], s[40:41], exec
	v_lshl_add_u32 v2, s56, 19, v239
	s_cselect_b32 s43, s45, s11
	s_cselect_b32 s59, s44, s10
	v_add_u32_e32 v245, v2, v238
	v_add_u32_e32 v246, v2, v240
	v_add_u32_e32 v212, v2, v241
	v_add_u32_e32 v214, v2, v242
	s_add_u32 s60, s10, 0x100
	v_mov_b32_e32 v2, 0
	v_mov_b32_e32 v213, v99
	v_mov_b32_e32 v215, v99
	s_addc_u32 s61, s11, 0
	s_mov_b32 s65, -2
	s_mov_b64 s[10:11], 0
	v_mov_b32_e32 v3, v2
	v_mov_b32_e32 v4, v2
	v_mov_b32_e32 v5, v2
	v_mov_b32_e32 v6, v2
	v_mov_b32_e32 v7, v2
	v_mov_b32_e32 v8, v2
	v_mov_b32_e32 v9, v2
	v_mov_b32_e32 v18, v2
	v_mov_b32_e32 v19, v2
	v_mov_b32_e32 v20, v2
	v_mov_b32_e32 v21, v2
	v_mov_b32_e32 v22, v2
	v_mov_b32_e32 v23, v2
	v_mov_b32_e32 v24, v2
	v_mov_b32_e32 v25, v2
	v_mov_b32_e32 v34, v2
	v_mov_b32_e32 v35, v2
	v_mov_b32_e32 v36, v2
	v_mov_b32_e32 v37, v2
	v_mov_b32_e32 v38, v2
	v_mov_b32_e32 v39, v2
	v_mov_b32_e32 v40, v2
	v_mov_b32_e32 v41, v2
	v_mov_b32_e32 v50, v2
	v_mov_b32_e32 v51, v2
	v_mov_b32_e32 v52, v2
	v_mov_b32_e32 v53, v2
	v_mov_b32_e32 v54, v2
	v_mov_b32_e32 v55, v2
	v_mov_b32_e32 v56, v2
	v_mov_b32_e32 v57, v2
	v_mov_b32_e32 v10, v2
	v_mov_b32_e32 v11, v2
	v_mov_b32_e32 v12, v2
	v_mov_b32_e32 v13, v2
	v_mov_b32_e32 v14, v2
	v_mov_b32_e32 v15, v2
	v_mov_b32_e32 v16, v2
	v_mov_b32_e32 v17, v2
	v_mov_b32_e32 v26, v2
	v_mov_b32_e32 v27, v2
	v_mov_b32_e32 v28, v2
	v_mov_b32_e32 v29, v2
	v_mov_b32_e32 v30, v2
	v_mov_b32_e32 v31, v2
	v_mov_b32_e32 v32, v2
	v_mov_b32_e32 v33, v2
	v_mov_b32_e32 v42, v2
	v_mov_b32_e32 v43, v2
	v_mov_b32_e32 v44, v2
	v_mov_b32_e32 v45, v2
	v_mov_b32_e32 v46, v2
	v_mov_b32_e32 v47, v2
	v_mov_b32_e32 v48, v2
	v_mov_b32_e32 v49, v2
	v_mov_b32_e32 v58, v2
	v_mov_b32_e32 v59, v2
	v_mov_b32_e32 v60, v2
	v_mov_b32_e32 v61, v2
	v_mov_b32_e32 v62, v2
	v_mov_b32_e32 v63, v2
	v_mov_b32_e32 v64, v2
	v_mov_b32_e32 v65, v2
	v_mov_b32_e32 v66, v2
	v_mov_b32_e32 v67, v2
	v_mov_b32_e32 v68, v2
	v_mov_b32_e32 v69, v2
	v_mov_b32_e32 v70, v2
	v_mov_b32_e32 v71, v2
	v_mov_b32_e32 v72, v2
	v_mov_b32_e32 v73, v2
	v_mov_b32_e32 v90, v2
	v_mov_b32_e32 v91, v2
	v_mov_b32_e32 v92, v2
	v_mov_b32_e32 v93, v2
	v_mov_b32_e32 v100, v2
	v_mov_b32_e32 v101, v2
	v_mov_b32_e32 v102, v2
	v_mov_b32_e32 v103, v2
	v_mov_b32_e32 v116, v2
	v_mov_b32_e32 v117, v2
	v_mov_b32_e32 v118, v2
	v_mov_b32_e32 v119, v2
	v_mov_b32_e32 v120, v2
	v_mov_b32_e32 v121, v2
	v_mov_b32_e32 v122, v2
	v_mov_b32_e32 v123, v2
	v_mov_b32_e32 v132, v2
	v_mov_b32_e32 v133, v2
	v_mov_b32_e32 v134, v2
	v_mov_b32_e32 v135, v2
	v_mov_b32_e32 v136, v2
	v_mov_b32_e32 v137, v2
	v_mov_b32_e32 v138, v2
	v_mov_b32_e32 v139, v2
	v_mov_b32_e32 v78, v2
	v_mov_b32_e32 v79, v2
	v_mov_b32_e32 v80, v2
	v_mov_b32_e32 v81, v2
	v_mov_b32_e32 v86, v2
	v_mov_b32_e32 v87, v2
	v_mov_b32_e32 v88, v2
	v_mov_b32_e32 v89, v2
	v_mov_b32_e32 v108, v2
	v_mov_b32_e32 v109, v2
	v_mov_b32_e32 v110, v2
	v_mov_b32_e32 v111, v2
	v_mov_b32_e32 v112, v2
	v_mov_b32_e32 v113, v2
	v_mov_b32_e32 v114, v2
	v_mov_b32_e32 v115, v2
	v_mov_b32_e32 v124, v2
	v_mov_b32_e32 v125, v2
	v_mov_b32_e32 v126, v2
	v_mov_b32_e32 v127, v2
	v_mov_b32_e32 v128, v2
	v_mov_b32_e32 v129, v2
	v_mov_b32_e32 v130, v2
	v_mov_b32_e32 v131, v2
	v_mov_b32_e32 v140, v2
	v_mov_b32_e32 v141, v2
	v_mov_b32_e32 v142, v2
	v_mov_b32_e32 v143, v2
	v_mov_b32_e32 v144, v2
	v_mov_b32_e32 v145, v2
	v_mov_b32_e32 v146, v2
	v_mov_b32_e32 v147, v2
	s_waitcnt vmcnt(8)
	v_mbcnt_lo_u32_b32 v3, -1, 0
	v_mbcnt_hi_u32_b32 v3, -1, v3
	v_readfirstlane_b32 s100, v0
	v_lshlrev_b32_e32 v3, 2, v3
	s_lshr_b32 s100, s100, 6
	s_and_b32 vcc_lo, s68, 1
	s_lshl_b32 vcc_lo, vcc_lo, 11
	s_add_i32 vcc_lo, vcc_lo, 0x22400
	s_cmp_gt_u32 s100, 3
	s_cbranch_scc1 .Linpf_cols
	s_lshl_b32 vcc_hi, s100, 8
	s_add_i32 m0, vcc_lo, vcc_hi
	s_lshl_b32 s101, s58, 10
	s_add_i32 s101, s101, vcc_hi
	s_add_u32 s100, s78, s101
	s_addc_u32 s101, s79, 0
	s_branch .Linpf_go

.LBB0_1504:
	s_ashr_i32 s41, s40, 31
	s_lshl_b64 s[10:11], s[40:41], 21
	s_add_u32 s31, s13, s10
	s_addc_u32 s41, s17, s11
	v_readlane_b32 s10, v253, 36
	v_readlane_b32 s11, v253, 37
	s_mov_b32 s46, s10
	s_ashr_i32 s47, s10, 31
	v_writelane_b32 v253, s10, 36
	v_lshl_add_u32 v2, s61, 18, v239
	v_mov_b32_e32 v66, 0
	v_writelane_b32 v253, s11, 37
	s_lshl_b64 s[10:11], s[46:47], 18
	s_add_u32 s10, s31, s10
	s_addc_u32 s11, s41, s11
	s_and_b64 s[46:47], s[8:9], exec
	s_cselect_b32 s41, s11, s45
	s_cselect_b32 s65, s10, s44
	s_add_u32 s66, s44, 0x100
	s_addc_u32 s68, s45, 0
	v_readlane_b32 s44, v253, 42
	v_add_u32_e32 v245, v2, v238
	v_add_u32_e32 v246, v240, v2
	v_add_u32_e32 v212, v241, v2
	v_add_u32_e32 v214, v242, v2
	v_mov_b32_e32 v213, v99
	v_mov_b32_e32 v215, v99
	s_mov_b32 s83, -2
	v_readlane_b32 s45, v253, 43
	v_mov_b32_e32 v67, v66
	v_mov_b32_e32 v68, v66
	v_mov_b32_e32 v69, v66
	v_mov_b32_e32 v70, v66
	v_mov_b32_e32 v71, v66
	v_mov_b32_e32 v72, v66
	v_mov_b32_e32 v73, v66
	v_mov_b32_e32 v74, v66
	v_mov_b32_e32 v75, v66
	v_mov_b32_e32 v76, v66
	v_mov_b32_e32 v77, v66
	v_mov_b32_e32 v78, v66
	v_mov_b32_e32 v79, v66
	v_mov_b32_e32 v80, v66
	v_mov_b32_e32 v81, v66
	v_mov_b32_e32 v82, v66
	v_mov_b32_e32 v83, v66
	v_mov_b32_e32 v84, v66
	v_mov_b32_e32 v85, v66
	v_mov_b32_e32 v86, v66
	v_mov_b32_e32 v87, v66
	v_mov_b32_e32 v88, v66
	v_mov_b32_e32 v89, v66
	v_mov_b32_e32 v90, v66
	v_mov_b32_e32 v91, v66
	v_mov_b32_e32 v92, v66
	v_mov_b32_e32 v93, v66
	v_mov_b32_e32 v94, v66
	v_mov_b32_e32 v95, v66
	v_mov_b32_e32 v96, v66
	v_mov_b32_e32 v97, v66
	v_mov_b32_e32 v124, v66
	v_mov_b32_e32 v125, v66
	v_mov_b32_e32 v126, v66
	v_mov_b32_e32 v127, v66
	v_mov_b32_e32 v132, v66
	v_mov_b32_e32 v133, v66
	v_mov_b32_e32 v134, v66
	v_mov_b32_e32 v135, v66
	v_mov_b32_e32 v140, v66
	v_mov_b32_e32 v141, v66
	v_mov_b32_e32 v142, v66
	v_mov_b32_e32 v143, v66
	v_mov_b32_e32 v144, v66
	v_mov_b32_e32 v145, v66
	v_mov_b32_e32 v146, v66
	v_mov_b32_e32 v147, v66
	v_mov_b32_e32 v148, v66
	v_mov_b32_e32 v149, v66
	v_mov_b32_e32 v150, v66
	v_mov_b32_e32 v151, v66
	v_mov_b32_e32 v152, v66
	v_mov_b32_e32 v153, v66
	v_mov_b32_e32 v154, v66
	v_mov_b32_e32 v155, v66
	v_mov_b32_e32 v156, v66
	v_mov_b32_e32 v157, v66
	v_mov_b32_e32 v158, v66
	v_mov_b32_e32 v159, v66
	v_mov_b32_e32 v160, v66
	v_mov_b32_e32 v161, v66
	v_mov_b32_e32 v162, v66
	v_mov_b32_e32 v163, v66
	v_mov_b32_e32 v100, v66
	v_mov_b32_e32 v101, v66
	v_mov_b32_e32 v102, v66
	v_mov_b32_e32 v103, v66
	v_mov_b32_e32 v104, v66
	v_mov_b32_e32 v105, v66
	v_mov_b32_e32 v106, v66
	v_mov_b32_e32 v107, v66
	v_mov_b32_e32 v108, v66
	v_mov_b32_e32 v109, v66
	v_mov_b32_e32 v110, v66
	v_mov_b32_e32 v111, v66
	v_mov_b32_e32 v112, v66
	v_mov_b32_e32 v113, v66
	v_mov_b32_e32 v114, v66
	v_mov_b32_e32 v115, v66
	v_mov_b32_e32 v116, v66
	v_mov_b32_e32 v117, v66
	v_mov_b32_e32 v118, v66
	v_mov_b32_e32 v119, v66
	v_mov_b32_e32 v120, v66
	v_mov_b32_e32 v121, v66
	v_mov_b32_e32 v122, v66
	v_mov_b32_e32 v123, v66
	v_mov_b32_e32 v128, v66
	v_mov_b32_e32 v129, v66
	v_mov_b32_e32 v130, v66
	v_mov_b32_e32 v131, v66
	v_mov_b32_e32 v136, v66
	v_mov_b32_e32 v137, v66
	v_mov_b32_e32 v138, v66
	v_mov_b32_e32 v139, v66
	v_mov_b32_e32 v164, v66
	v_mov_b32_e32 v165, v66
	v_mov_b32_e32 v166, v66
	v_mov_b32_e32 v167, v66
	v_mov_b32_e32 v168, v66
	v_mov_b32_e32 v169, v66
	v_mov_b32_e32 v170, v66
	v_mov_b32_e32 v171, v66
	v_mov_b32_e32 v172, v66
	v_mov_b32_e32 v173, v66
	v_mov_b32_e32 v174, v66
	v_mov_b32_e32 v175, v66
	v_mov_b32_e32 v176, v66
	v_mov_b32_e32 v177, v66
	v_mov_b32_e32 v178, v66
	v_mov_b32_e32 v179, v66
	v_mov_b32_e32 v180, v66
	v_mov_b32_e32 v181, v66
	v_mov_b32_e32 v182, v66
	v_mov_b32_e32 v183, v66
	v_mov_b32_e32 v184, v66
	v_mov_b32_e32 v185, v66
	v_mov_b32_e32 v186, v66
	v_mov_b32_e32 v187, v66
	v_mov_b32_e32 v188, v66
	v_mov_b32_e32 v189, v66
	v_mov_b32_e32 v190, v66
	v_mov_b32_e32 v191, v66
	v_mov_b32_e32 v192, v66
	v_mov_b32_e32 v193, v66
	v_mov_b32_e32 v194, v66
	v_mov_b32_e32 v195, v66
	s_waitcnt vmcnt(16)
	v_mbcnt_lo_u32_b32 v3, -1, 0
	v_mbcnt_hi_u32_b32 v3, -1, v3
	v_readfirstlane_b32 s100, v0
	v_lshlrev_b32_e32 v3, 2, v3
	s_lshr_b32 s100, s100, 6
	s_and_b32 vcc_lo, s60, 1
	s_lshl_b32 vcc_lo, vcc_lo, 11
	s_add_i32 vcc_lo, vcc_lo, 0x20c00
	s_cmp_gt_u32 s100, 3
	s_cbranch_scc1 .Lg2pf_bias
	s_lshl_b32 vcc_hi, s100, 8
	s_add_i32 m0, vcc_lo, vcc_hi
	s_lshl_b32 s101, s43, 10
	s_add_i32 s101, s101, vcc_hi
	s_add_u32 s100, s70, s101
	s_addc_u32 s101, s71, 0
	s_branch .Lg2pf_go
